# P8 fast epilogue: row scales read in use order with counted lgkmcnt per row group (on top of v85)
# baseline (speedup 1.0000x reference)
.Lp8fast:
	ds_read_b32 v192, v176
	ds_read_b32 v178, v176 offset:64
	ds_read_b32 v180, v176 offset:128
	ds_read_b32 v182, v176 offset:192
	ds_read_b32 v184, v176 offset:512
	ds_read_b32 v186, v176 offset:576
	ds_read_b32 v188, v176 offset:640
	ds_read_b32 v190, v176 offset:704
	s_lshl_b32 s22, s22, 7
	s_ashr_i32 s23, s22, 31
	s_mov_b32 s26, 0xbfb8aa3b
	v_mov_b64_e32 v[218:219], s[8:9]
	v_mad_u64_u32 v[218:219], s[24:25], v166, s53, v[218:219]
	v_mov_b32_e32 v220, v219
	v_mad_u64_u32 v[220:221], s[24:25], v167, s53, v[220:221]
	v_mov_b32_e32 v219, v220
	v_lshl_add_u64 v[218:219], s[22:23], 1, v[218:219]
	v_lshl_add_u64 v[218:219], v[218:219], 0, v[154:155]
	s_waitcnt lgkmcnt(7)
	v_pk_fma_f32 v[142:143], v[142:143], v[192:193], v[78:79] op_sel_hi:[1,0,1]
	v_pk_fma_f32 v[144:145], v[144:145], v[192:193], v[80:81] op_sel_hi:[1,0,1]
	v_pk_fma_f32 v[138:139], v[138:139], v[192:193], v[74:75] op_sel_hi:[1,0,1]
	v_pk_fma_f32 v[140:141], v[140:141], v[192:193], v[76:77] op_sel_hi:[1,0,1]
	v_pk_fma_f32 v[134:135], v[134:135], v[192:193], v[62:63] op_sel_hi:[1,0,1]
	v_pk_fma_f32 v[136:137], v[136:137], v[192:193], v[64:65] op_sel_hi:[1,0,1]
	v_pk_fma_f32 v[130:131], v[130:131], v[192:193], v[58:59] op_sel_hi:[1,0,1]
	v_pk_fma_f32 v[132:133], v[132:133], v[192:193], v[60:61] op_sel_hi:[1,0,1]
	v_pk_mul_f32 v[192:193], v[138:139], s[26:27] op_sel_hi:[1,0]
	v_pk_mul_f32 v[194:195], v[140:141], s[26:27] op_sel_hi:[1,0]
	v_pk_mul_f32 v[196:197], v[142:143], s[26:27] op_sel_hi:[1,0]
	v_pk_mul_f32 v[198:199], v[144:145], s[26:27] op_sel_hi:[1,0]
	v_exp_f32_e32 v192, v192
	v_exp_f32_e32 v193, v193
	v_exp_f32_e32 v194, v194
	v_exp_f32_e32 v195, v195
	v_exp_f32_e32 v196, v196
	v_exp_f32_e32 v197, v197
	v_exp_f32_e32 v198, v198
	v_exp_f32_e32 v199, v199
	v_add_f32_e32 v192, 1.0, v192
	v_add_f32_e32 v193, 1.0, v193
	v_add_f32_e32 v194, 1.0, v194
	v_add_f32_e32 v195, 1.0, v195
	v_add_f32_e32 v196, 1.0, v196
	v_add_f32_e32 v197, 1.0, v197
	v_add_f32_e32 v198, 1.0, v198
	v_add_f32_e32 v199, 1.0, v199
	v_rcp_f32_e32 v192, v192
	v_rcp_f32_e32 v193, v193
	v_rcp_f32_e32 v194, v194
	v_rcp_f32_e32 v195, v195
	v_rcp_f32_e32 v196, v196
	v_rcp_f32_e32 v197, v197
	v_rcp_f32_e32 v198, v198
	v_rcp_f32_e32 v199, v199
	v_pk_mul_f32 v[192:193], v[138:139], v[192:193]
	v_pk_mul_f32 v[194:195], v[140:141], v[194:195]
	v_pk_mul_f32 v[196:197], v[142:143], v[196:197]
	v_pk_mul_f32 v[198:199], v[144:145], v[198:199]
	v_pk_mul_f32 v[202:203], v[192:193], v[130:131]
	v_pk_mul_f32 v[204:205], v[194:195], v[132:133]
	v_pk_mul_f32 v[206:207], v[196:197], v[134:135]
	v_pk_mul_f32 v[208:209], v[198:199], v[136:137]
	v_cvt_pk_bf16_f32 v210, v206, v207
	v_cvt_pk_bf16_f32 v211, v208, v209
	v_cvt_pk_bf16_f32 v212, v202, v203
	v_cvt_pk_bf16_f32 v213, v204, v205
	global_store_dwordx4 v[218:219], v[210:213], off
	v_add_co_u32_e32 v218, vcc, 0x16000, v218
	s_nop 1
	v_addc_co_u32_e32 v219, vcc, 0, v219, vcc
	s_waitcnt lgkmcnt(6)
	v_pk_fma_f32 v[126:127], v[126:127], v[178:179], v[78:79] op_sel_hi:[1,0,1]
	v_pk_fma_f32 v[128:129], v[128:129], v[178:179], v[80:81] op_sel_hi:[1,0,1]
	v_pk_fma_f32 v[122:123], v[122:123], v[178:179], v[74:75] op_sel_hi:[1,0,1]
	v_pk_fma_f32 v[124:125], v[124:125], v[178:179], v[76:77] op_sel_hi:[1,0,1]
	v_pk_fma_f32 v[118:119], v[118:119], v[178:179], v[62:63] op_sel_hi:[1,0,1]
	v_pk_fma_f32 v[120:121], v[120:121], v[178:179], v[64:65] op_sel_hi:[1,0,1]
	v_pk_fma_f32 v[114:115], v[114:115], v[178:179], v[58:59] op_sel_hi:[1,0,1]
	v_pk_fma_f32 v[116:117], v[116:117], v[178:179], v[60:61] op_sel_hi:[1,0,1]
	v_pk_mul_f32 v[192:193], v[122:123], s[26:27] op_sel_hi:[1,0]
	v_pk_mul_f32 v[194:195], v[124:125], s[26:27] op_sel_hi:[1,0]
	v_pk_mul_f32 v[196:197], v[126:127], s[26:27] op_sel_hi:[1,0]
	v_pk_mul_f32 v[198:199], v[128:129], s[26:27] op_sel_hi:[1,0]
	v_exp_f32_e32 v192, v192
	v_exp_f32_e32 v193, v193
	v_exp_f32_e32 v194, v194
	v_exp_f32_e32 v195, v195
	v_exp_f32_e32 v196, v196
	v_exp_f32_e32 v197, v197
	v_exp_f32_e32 v198, v198
	v_exp_f32_e32 v199, v199
	v_add_f32_e32 v192, 1.0, v192
	v_add_f32_e32 v193, 1.0, v193
	v_add_f32_e32 v194, 1.0, v194
	v_add_f32_e32 v195, 1.0, v195
	v_add_f32_e32 v196, 1.0, v196
	v_add_f32_e32 v197, 1.0, v197
	v_add_f32_e32 v198, 1.0, v198
	v_add_f32_e32 v199, 1.0, v199
	v_rcp_f32_e32 v192, v192
	v_rcp_f32_e32 v193, v193
	v_rcp_f32_e32 v194, v194
	v_rcp_f32_e32 v195, v195
	v_rcp_f32_e32 v196, v196
	v_rcp_f32_e32 v197, v197
	v_rcp_f32_e32 v198, v198
	v_rcp_f32_e32 v199, v199
	v_pk_mul_f32 v[192:193], v[122:123], v[192:193]
	v_pk_mul_f32 v[194:195], v[124:125], v[194:195]
	v_pk_mul_f32 v[196:197], v[126:127], v[196:197]
	v_pk_mul_f32 v[198:199], v[128:129], v[198:199]
	v_pk_mul_f32 v[202:203], v[192:193], v[114:115]
	v_pk_mul_f32 v[204:205], v[194:195], v[116:117]
	v_pk_mul_f32 v[206:207], v[196:197], v[118:119]
	v_pk_mul_f32 v[208:209], v[198:199], v[120:121]
	v_cvt_pk_bf16_f32 v210, v206, v207
	v_cvt_pk_bf16_f32 v211, v208, v209
	v_cvt_pk_bf16_f32 v212, v202, v203
	v_cvt_pk_bf16_f32 v213, v204, v205
	global_store_dwordx4 v[218:219], v[210:213], off
	v_add_co_u32_e32 v218, vcc, 0x16000, v218
	s_nop 1
	v_addc_co_u32_e32 v219, vcc, 0, v219, vcc
	s_waitcnt lgkmcnt(5)
	v_pk_fma_f32 v[110:111], v[110:111], v[180:181], v[78:79] op_sel_hi:[1,0,1]
	v_pk_fma_f32 v[112:113], v[112:113], v[180:181], v[80:81] op_sel_hi:[1,0,1]
	v_pk_fma_f32 v[106:107], v[106:107], v[180:181], v[74:75] op_sel_hi:[1,0,1]
	v_pk_fma_f32 v[108:109], v[108:109], v[180:181], v[76:77] op_sel_hi:[1,0,1]
	v_pk_fma_f32 v[102:103], v[102:103], v[180:181], v[62:63] op_sel_hi:[1,0,1]
	v_pk_fma_f32 v[104:105], v[104:105], v[180:181], v[64:65] op_sel_hi:[1,0,1]
	v_pk_fma_f32 v[98:99], v[98:99], v[180:181], v[58:59] op_sel_hi:[1,0,1]
	v_pk_fma_f32 v[100:101], v[100:101], v[180:181], v[60:61] op_sel_hi:[1,0,1]
	v_pk_mul_f32 v[192:193], v[106:107], s[26:27] op_sel_hi:[1,0]
	v_pk_mul_f32 v[194:195], v[108:109], s[26:27] op_sel_hi:[1,0]
	v_pk_mul_f32 v[196:197], v[110:111], s[26:27] op_sel_hi:[1,0]
	v_pk_mul_f32 v[198:199], v[112:113], s[26:27] op_sel_hi:[1,0]
	v_exp_f32_e32 v192, v192
	v_exp_f32_e32 v193, v193
	v_exp_f32_e32 v194, v194
	v_exp_f32_e32 v195, v195
	v_exp_f32_e32 v196, v196
	v_exp_f32_e32 v197, v197
	v_exp_f32_e32 v198, v198
	v_exp_f32_e32 v199, v199
	v_add_f32_e32 v192, 1.0, v192
	v_add_f32_e32 v193, 1.0, v193
	v_add_f32_e32 v194, 1.0, v194
	v_add_f32_e32 v195, 1.0, v195
	v_add_f32_e32 v196, 1.0, v196
	v_add_f32_e32 v197, 1.0, v197
	v_add_f32_e32 v198, 1.0, v198
	v_add_f32_e32 v199, 1.0, v199
	v_rcp_f32_e32 v192, v192
	v_rcp_f32_e32 v193, v193
	v_rcp_f32_e32 v194, v194
	v_rcp_f32_e32 v195, v195
	v_rcp_f32_e32 v196, v196
	v_rcp_f32_e32 v197, v197
	v_rcp_f32_e32 v198, v198
	v_rcp_f32_e32 v199, v199
	v_pk_mul_f32 v[192:193], v[106:107], v[192:193]
	v_pk_mul_f32 v[194:195], v[108:109], v[194:195]
	v_pk_mul_f32 v[196:197], v[110:111], v[196:197]
	v_pk_mul_f32 v[198:199], v[112:113], v[198:199]
	v_pk_mul_f32 v[202:203], v[192:193], v[98:99]
	v_pk_mul_f32 v[204:205], v[194:195], v[100:101]
	v_pk_mul_f32 v[206:207], v[196:197], v[102:103]
	v_pk_mul_f32 v[208:209], v[198:199], v[104:105]
	v_cvt_pk_bf16_f32 v210, v206, v207
	v_cvt_pk_bf16_f32 v211, v208, v209
	v_cvt_pk_bf16_f32 v212, v202, v203
	v_cvt_pk_bf16_f32 v213, v204, v205
	global_store_dwordx4 v[218:219], v[210:213], off
	v_add_co_u32_e32 v218, vcc, 0x16000, v218
	s_nop 1
	v_addc_co_u32_e32 v219, vcc, 0, v219, vcc
	s_waitcnt lgkmcnt(4)
	v_pk_fma_f32 v[94:95], v[94:95], v[182:183], v[78:79] op_sel_hi:[1,0,1]
	v_pk_fma_f32 v[96:97], v[96:97], v[182:183], v[80:81] op_sel_hi:[1,0,1]
	v_pk_fma_f32 v[90:91], v[90:91], v[182:183], v[74:75] op_sel_hi:[1,0,1]
	v_pk_fma_f32 v[92:93], v[92:93], v[182:183], v[76:77] op_sel_hi:[1,0,1]
	v_pk_fma_f32 v[86:87], v[86:87], v[182:183], v[62:63] op_sel_hi:[1,0,1]
	v_pk_fma_f32 v[88:89], v[88:89], v[182:183], v[64:65] op_sel_hi:[1,0,1]
	v_pk_fma_f32 v[82:83], v[82:83], v[182:183], v[58:59] op_sel_hi:[1,0,1]
	v_pk_fma_f32 v[84:85], v[84:85], v[182:183], v[60:61] op_sel_hi:[1,0,1]
	v_pk_mul_f32 v[192:193], v[90:91], s[26:27] op_sel_hi:[1,0]
	v_pk_mul_f32 v[194:195], v[92:93], s[26:27] op_sel_hi:[1,0]
	v_pk_mul_f32 v[196:197], v[94:95], s[26:27] op_sel_hi:[1,0]
	v_pk_mul_f32 v[198:199], v[96:97], s[26:27] op_sel_hi:[1,0]
	v_exp_f32_e32 v192, v192
	v_exp_f32_e32 v193, v193
	v_exp_f32_e32 v194, v194
	v_exp_f32_e32 v195, v195
	v_exp_f32_e32 v196, v196
	v_exp_f32_e32 v197, v197
	v_exp_f32_e32 v198, v198
	v_exp_f32_e32 v199, v199
	v_add_f32_e32 v192, 1.0, v192
	v_add_f32_e32 v193, 1.0, v193
	v_add_f32_e32 v194, 1.0, v194
	v_add_f32_e32 v195, 1.0, v195
	v_add_f32_e32 v196, 1.0, v196
	v_add_f32_e32 v197, 1.0, v197
	v_add_f32_e32 v198, 1.0, v198
	v_add_f32_e32 v199, 1.0, v199
	v_rcp_f32_e32 v192, v192
	v_rcp_f32_e32 v193, v193
	v_rcp_f32_e32 v194, v194
	v_rcp_f32_e32 v195, v195
	v_rcp_f32_e32 v196, v196
	v_rcp_f32_e32 v197, v197
	v_rcp_f32_e32 v198, v198
	v_rcp_f32_e32 v199, v199
	v_pk_mul_f32 v[192:193], v[90:91], v[192:193]
	v_pk_mul_f32 v[194:195], v[92:93], v[194:195]
	v_pk_mul_f32 v[196:197], v[94:95], v[196:197]
	v_pk_mul_f32 v[198:199], v[96:97], v[198:199]
	v_pk_mul_f32 v[202:203], v[192:193], v[82:83]
	v_pk_mul_f32 v[204:205], v[194:195], v[84:85]
	v_pk_mul_f32 v[206:207], v[196:197], v[86:87]
	v_pk_mul_f32 v[208:209], v[198:199], v[88:89]
	v_cvt_pk_bf16_f32 v210, v206, v207
	v_cvt_pk_bf16_f32 v211, v208, v209
	v_cvt_pk_bf16_f32 v212, v202, v203
	v_cvt_pk_bf16_f32 v213, v204, v205
	global_store_dwordx4 v[218:219], v[210:213], off
	v_add_co_u32_e32 v218, vcc, 0x6e000, v218
	s_nop 1
	v_addc_co_u32_e32 v219, vcc, 0, v219, vcc
	s_waitcnt lgkmcnt(3)
	v_pk_fma_f32 v[70:71], v[70:71], v[184:185], v[78:79] op_sel_hi:[1,0,1]
	v_pk_fma_f32 v[72:73], v[72:73], v[184:185], v[80:81] op_sel_hi:[1,0,1]
	v_pk_fma_f32 v[66:67], v[66:67], v[184:185], v[74:75] op_sel_hi:[1,0,1]
	v_pk_fma_f32 v[68:69], v[68:69], v[184:185], v[76:77] op_sel_hi:[1,0,1]
	v_pk_fma_f32 v[54:55], v[54:55], v[184:185], v[62:63] op_sel_hi:[1,0,1]
	v_pk_fma_f32 v[56:57], v[56:57], v[184:185], v[64:65] op_sel_hi:[1,0,1]
	v_pk_fma_f32 v[50:51], v[50:51], v[184:185], v[58:59] op_sel_hi:[1,0,1]
	v_pk_fma_f32 v[52:53], v[52:53], v[184:185], v[60:61] op_sel_hi:[1,0,1]
	v_pk_mul_f32 v[192:193], v[66:67], s[26:27] op_sel_hi:[1,0]
	v_pk_mul_f32 v[194:195], v[68:69], s[26:27] op_sel_hi:[1,0]
	v_pk_mul_f32 v[196:197], v[70:71], s[26:27] op_sel_hi:[1,0]
	v_pk_mul_f32 v[198:199], v[72:73], s[26:27] op_sel_hi:[1,0]
	v_exp_f32_e32 v192, v192
	v_exp_f32_e32 v193, v193
	v_exp_f32_e32 v194, v194
	v_exp_f32_e32 v195, v195
	v_exp_f32_e32 v196, v196
	v_exp_f32_e32 v197, v197
	v_exp_f32_e32 v198, v198
	v_exp_f32_e32 v199, v199
	v_add_f32_e32 v192, 1.0, v192
	v_add_f32_e32 v193, 1.0, v193
	v_add_f32_e32 v194, 1.0, v194
	v_add_f32_e32 v195, 1.0, v195
	v_add_f32_e32 v196, 1.0, v196
	v_add_f32_e32 v197, 1.0, v197
	v_add_f32_e32 v198, 1.0, v198
	v_add_f32_e32 v199, 1.0, v199
	v_rcp_f32_e32 v192, v192
	v_rcp_f32_e32 v193, v193
	v_rcp_f32_e32 v194, v194
	v_rcp_f32_e32 v195, v195
	v_rcp_f32_e32 v196, v196
	v_rcp_f32_e32 v197, v197
	v_rcp_f32_e32 v198, v198
	v_rcp_f32_e32 v199, v199
	v_pk_mul_f32 v[192:193], v[66:67], v[192:193]
	v_pk_mul_f32 v[194:195], v[68:69], v[194:195]
	v_pk_mul_f32 v[196:197], v[70:71], v[196:197]
	v_pk_mul_f32 v[198:199], v[72:73], v[198:199]
	v_pk_mul_f32 v[202:203], v[192:193], v[50:51]
	v_pk_mul_f32 v[204:205], v[194:195], v[52:53]
	v_pk_mul_f32 v[206:207], v[196:197], v[54:55]
	v_pk_mul_f32 v[208:209], v[198:199], v[56:57]
	v_cvt_pk_bf16_f32 v210, v206, v207
	v_cvt_pk_bf16_f32 v211, v208, v209
	v_cvt_pk_bf16_f32 v212, v202, v203
	v_cvt_pk_bf16_f32 v213, v204, v205
	global_store_dwordx4 v[218:219], v[210:213], off
	v_add_co_u32_e32 v218, vcc, 0x16000, v218
	s_nop 1
	v_addc_co_u32_e32 v219, vcc, 0, v219, vcc
	s_waitcnt lgkmcnt(2)
	v_pk_fma_f32 v[46:47], v[46:47], v[186:187], v[78:79] op_sel_hi:[1,0,1]
	v_pk_fma_f32 v[48:49], v[48:49], v[186:187], v[80:81] op_sel_hi:[1,0,1]
	v_pk_fma_f32 v[42:43], v[42:43], v[186:187], v[74:75] op_sel_hi:[1,0,1]
	v_pk_fma_f32 v[44:45], v[44:45], v[186:187], v[76:77] op_sel_hi:[1,0,1]
	v_pk_fma_f32 v[38:39], v[38:39], v[186:187], v[62:63] op_sel_hi:[1,0,1]
	v_pk_fma_f32 v[40:41], v[40:41], v[186:187], v[64:65] op_sel_hi:[1,0,1]
	v_pk_fma_f32 v[34:35], v[34:35], v[186:187], v[58:59] op_sel_hi:[1,0,1]
	v_pk_fma_f32 v[36:37], v[36:37], v[186:187], v[60:61] op_sel_hi:[1,0,1]
	v_pk_mul_f32 v[192:193], v[42:43], s[26:27] op_sel_hi:[1,0]
	v_pk_mul_f32 v[194:195], v[44:45], s[26:27] op_sel_hi:[1,0]
	v_pk_mul_f32 v[196:197], v[46:47], s[26:27] op_sel_hi:[1,0]
	v_pk_mul_f32 v[198:199], v[48:49], s[26:27] op_sel_hi:[1,0]
	v_exp_f32_e32 v192, v192
	v_exp_f32_e32 v193, v193
	v_exp_f32_e32 v194, v194
	v_exp_f32_e32 v195, v195
	v_exp_f32_e32 v196, v196
	v_exp_f32_e32 v197, v197
	v_exp_f32_e32 v198, v198
	v_exp_f32_e32 v199, v199
	v_add_f32_e32 v192, 1.0, v192
	v_add_f32_e32 v193, 1.0, v193
	v_add_f32_e32 v194, 1.0, v194
	v_add_f32_e32 v195, 1.0, v195
	v_add_f32_e32 v196, 1.0, v196
	v_add_f32_e32 v197, 1.0, v197
	v_add_f32_e32 v198, 1.0, v198
	v_add_f32_e32 v199, 1.0, v199
	v_rcp_f32_e32 v192, v192
	v_rcp_f32_e32 v193, v193
	v_rcp_f32_e32 v194, v194
	v_rcp_f32_e32 v195, v195
	v_rcp_f32_e32 v196, v196
	v_rcp_f32_e32 v197, v197
	v_rcp_f32_e32 v198, v198
	v_rcp_f32_e32 v199, v199
	v_pk_mul_f32 v[192:193], v[42:43], v[192:193]
	v_pk_mul_f32 v[194:195], v[44:45], v[194:195]
	v_pk_mul_f32 v[196:197], v[46:47], v[196:197]
	v_pk_mul_f32 v[198:199], v[48:49], v[198:199]
	v_pk_mul_f32 v[202:203], v[192:193], v[34:35]
	v_pk_mul_f32 v[204:205], v[194:195], v[36:37]
	v_pk_mul_f32 v[206:207], v[196:197], v[38:39]
	v_pk_mul_f32 v[208:209], v[198:199], v[40:41]
	v_cvt_pk_bf16_f32 v210, v206, v207
	v_cvt_pk_bf16_f32 v211, v208, v209
	v_cvt_pk_bf16_f32 v212, v202, v203
	v_cvt_pk_bf16_f32 v213, v204, v205
	global_store_dwordx4 v[218:219], v[210:213], off
	v_add_co_u32_e32 v218, vcc, 0x16000, v218
	s_nop 1
	v_addc_co_u32_e32 v219, vcc, 0, v219, vcc
	s_waitcnt lgkmcnt(1)
	v_pk_fma_f32 v[30:31], v[30:31], v[188:189], v[78:79] op_sel_hi:[1,0,1]
	v_pk_fma_f32 v[32:33], v[32:33], v[188:189], v[80:81] op_sel_hi:[1,0,1]
	v_pk_fma_f32 v[26:27], v[26:27], v[188:189], v[74:75] op_sel_hi:[1,0,1]
	v_pk_fma_f32 v[28:29], v[28:29], v[188:189], v[76:77] op_sel_hi:[1,0,1]
	v_pk_fma_f32 v[22:23], v[22:23], v[188:189], v[62:63] op_sel_hi:[1,0,1]
	v_pk_fma_f32 v[24:25], v[24:25], v[188:189], v[64:65] op_sel_hi:[1,0,1]
	v_pk_fma_f32 v[18:19], v[18:19], v[188:189], v[58:59] op_sel_hi:[1,0,1]
	v_pk_fma_f32 v[20:21], v[20:21], v[188:189], v[60:61] op_sel_hi:[1,0,1]
	v_pk_mul_f32 v[192:193], v[26:27], s[26:27] op_sel_hi:[1,0]
	v_pk_mul_f32 v[194:195], v[28:29], s[26:27] op_sel_hi:[1,0]
	v_pk_mul_f32 v[196:197], v[30:31], s[26:27] op_sel_hi:[1,0]
	v_pk_mul_f32 v[198:199], v[32:33], s[26:27] op_sel_hi:[1,0]
	v_exp_f32_e32 v192, v192
	v_exp_f32_e32 v193, v193
	v_exp_f32_e32 v194, v194
	v_exp_f32_e32 v195, v195
	v_exp_f32_e32 v196, v196
	v_exp_f32_e32 v197, v197
	v_exp_f32_e32 v198, v198
	v_exp_f32_e32 v199, v199
	v_add_f32_e32 v192, 1.0, v192
	v_add_f32_e32 v193, 1.0, v193
	v_add_f32_e32 v194, 1.0, v194
	v_add_f32_e32 v195, 1.0, v195
	v_add_f32_e32 v196, 1.0, v196
	v_add_f32_e32 v197, 1.0, v197
	v_add_f32_e32 v198, 1.0, v198
	v_add_f32_e32 v199, 1.0, v199
	v_rcp_f32_e32 v192, v192
	v_rcp_f32_e32 v193, v193
	v_rcp_f32_e32 v194, v194
	v_rcp_f32_e32 v195, v195
	v_rcp_f32_e32 v196, v196
	v_rcp_f32_e32 v197, v197
	v_rcp_f32_e32 v198, v198
	v_rcp_f32_e32 v199, v199
	v_pk_mul_f32 v[192:193], v[26:27], v[192:193]
	v_pk_mul_f32 v[194:195], v[28:29], v[194:195]
	v_pk_mul_f32 v[196:197], v[30:31], v[196:197]
	v_pk_mul_f32 v[198:199], v[32:33], v[198:199]
	v_pk_mul_f32 v[202:203], v[192:193], v[18:19]
	v_pk_mul_f32 v[204:205], v[194:195], v[20:21]
	v_pk_mul_f32 v[206:207], v[196:197], v[22:23]
	v_pk_mul_f32 v[208:209], v[198:199], v[24:25]
	v_cvt_pk_bf16_f32 v210, v206, v207
	v_cvt_pk_bf16_f32 v211, v208, v209
	v_cvt_pk_bf16_f32 v212, v202, v203
	v_cvt_pk_bf16_f32 v213, v204, v205
	global_store_dwordx4 v[218:219], v[210:213], off
	v_add_co_u32_e32 v218, vcc, 0x16000, v218
	s_nop 1
	v_addc_co_u32_e32 v219, vcc, 0, v219, vcc
	s_waitcnt lgkmcnt(0)
	v_pk_fma_f32 v[14:15], v[14:15], v[190:191], v[78:79] op_sel_hi:[1,0,1]
	v_pk_fma_f32 v[16:17], v[16:17], v[190:191], v[80:81] op_sel_hi:[1,0,1]
	v_pk_fma_f32 v[10:11], v[10:11], v[190:191], v[74:75] op_sel_hi:[1,0,1]
	v_pk_fma_f32 v[12:13], v[12:13], v[190:191], v[76:77] op_sel_hi:[1,0,1]
	v_pk_fma_f32 v[6:7], v[6:7], v[190:191], v[62:63] op_sel_hi:[1,0,1]
	v_pk_fma_f32 v[8:9], v[8:9], v[190:191], v[64:65] op_sel_hi:[1,0,1]
	v_pk_fma_f32 v[2:3], v[2:3], v[190:191], v[58:59] op_sel_hi:[1,0,1]
	v_pk_fma_f32 v[4:5], v[4:5], v[190:191], v[60:61] op_sel_hi:[1,0,1]
	v_pk_mul_f32 v[192:193], v[10:11], s[26:27] op_sel_hi:[1,0]
	v_pk_mul_f32 v[194:195], v[12:13], s[26:27] op_sel_hi:[1,0]
	v_pk_mul_f32 v[196:197], v[14:15], s[26:27] op_sel_hi:[1,0]
	v_pk_mul_f32 v[198:199], v[16:17], s[26:27] op_sel_hi:[1,0]
	v_exp_f32_e32 v192, v192
	v_exp_f32_e32 v193, v193
	v_exp_f32_e32 v194, v194
	v_exp_f32_e32 v195, v195
	v_exp_f32_e32 v196, v196
	v_exp_f32_e32 v197, v197
	v_exp_f32_e32 v198, v198
	v_exp_f32_e32 v199, v199
	v_add_f32_e32 v192, 1.0, v192
	v_add_f32_e32 v193, 1.0, v193
	v_add_f32_e32 v194, 1.0, v194
	v_add_f32_e32 v195, 1.0, v195
	v_add_f32_e32 v196, 1.0, v196
	v_add_f32_e32 v197, 1.0, v197
	v_add_f32_e32 v198, 1.0, v198
	v_add_f32_e32 v199, 1.0, v199
	v_rcp_f32_e32 v192, v192
	v_rcp_f32_e32 v193, v193
	v_rcp_f32_e32 v194, v194
	v_rcp_f32_e32 v195, v195
	v_rcp_f32_e32 v196, v196
	v_rcp_f32_e32 v197, v197
	v_rcp_f32_e32 v198, v198
	v_rcp_f32_e32 v199, v199
	v_pk_mul_f32 v[192:193], v[10:11], v[192:193]
	v_pk_mul_f32 v[194:195], v[12:13], v[194:195]
	v_pk_mul_f32 v[196:197], v[14:15], v[196:197]
	v_pk_mul_f32 v[198:199], v[16:17], v[198:199]
	v_pk_mul_f32 v[202:203], v[192:193], v[2:3]
	v_pk_mul_f32 v[204:205], v[194:195], v[4:5]
	v_pk_mul_f32 v[206:207], v[196:197], v[6:7]
	v_pk_mul_f32 v[208:209], v[198:199], v[8:9]
	v_cvt_pk_bf16_f32 v210, v206, v207
	v_cvt_pk_bf16_f32 v211, v208, v209
	v_cvt_pk_bf16_f32 v212, v202, v203
	v_cvt_pk_bf16_f32 v213, v204, v205
	global_store_dwordx4 v[218:219], v[210:213], off
	s_andn2_b64 vcc, exec, s[4:5]
	s_mov_b64 s[4:5], -1
	s_branch .Lp8_tail
